# v72 + S5 scan: LAM16 load hoisted above the barriers; XP store drain before GEMM2 removed (in-order counted waits of the prologue cover it; XP tile is first loaded after the prologue barrier)
# baseline (speedup 1.0000x reference)
.LBB0_783:
	s_nop 6
	v_and_b32_e32 v7, 63, v36
	s_lshl_b32 s12, s53, 7
	v_ashrrev_i32_e32 v3, 6, v36
	s_or_b32 s12, s12, s20
	v_lshlrev_b32_e32 v9, 1, v7
	v_readlane_b32 s18, v248, 38
	v_or_b32_e32 v4, s12, v9
	v_mov_b32_e32 v5, v2
	v_readlane_b32 s19, v248, 39
	v_lshlrev_b32_e32 v6, 13, v3
	s_add_i32 s12, 0, 0x10000
	v_lshlrev_b32_e32 v8, 2, v7
	v_lshl_add_u64 v[4:5], v[4:5], 2, s[18:19]
	global_load_dwordx2 v[4:5], v[4:5], off
	v_add3_u32 v6, s12, v6, v8
	s_waitcnt lgkmcnt(0)
	s_barrier
	s_barrier
	ds_read2st64_b32 v[10:11], v6 offset1:1
	ds_read2st64_b32 v[12:13], v6 offset0:2 offset1:3
	ds_read2st64_b32 v[14:15], v6 offset0:4 offset1:5
	ds_read2st64_b32 v[16:17], v6 offset0:6 offset1:7
	ds_read2st64_b32 v[18:19], v6 offset0:8 offset1:9
	ds_read2st64_b32 v[20:21], v6 offset0:10 offset1:11
	ds_read2st64_b32 v[22:23], v6 offset0:12 offset1:13
	ds_read2st64_b32 v[24:25], v6 offset0:14 offset1:15
	ds_read2st64_b32 v[26:27], v6 offset0:16 offset1:17
	ds_read2st64_b32 v[54:55], v6 offset0:18 offset1:19
	ds_read2st64_b32 v[56:57], v6 offset0:20 offset1:21
	ds_read2st64_b32 v[58:59], v6 offset0:22 offset1:23
	ds_read2st64_b32 v[60:61], v6 offset0:24 offset1:25
	ds_read2st64_b32 v[62:63], v6 offset0:26 offset1:27
	ds_read2st64_b32 v[64:65], v6 offset0:28 offset1:29
	ds_read2st64_b32 v[66:67], v6 offset0:30 offset1:31
	v_lshl_add_u32 v31, v36, 3, 0
	v_cmp_lt_i32_e32 vcc, 0, v3
	s_waitcnt vmcnt(0)
	v_mul_f32_e32 v52, 0, v5
	v_mul_f32_e32 v53, 0, v4
	v_fmac_f32_e32 v52, 0, v4
	v_fmac_f32_e32 v53, 0x80000000, v5
	s_waitcnt lgkmcnt(14)
	v_add_f32_e32 v48, v52, v11
	v_add_f32_e32 v50, v53, v10
	v_pk_mul_f32 v[10:11], v[4:5], v[48:49] op_sel:[1,0] op_sel_hi:[0,0]
	v_pk_fma_f32 v[28:29], v[4:5], v[50:51], v[10:11] neg_lo:[0,0,1] neg_hi:[0,0,1]
	v_pk_fma_f32 v[10:11], v[4:5], v[50:51], v[10:11] op_sel_hi:[1,0,1]
	s_nop 0
	v_mov_b32_e32 v29, v11
	v_pk_add_f32 v[46:47], v[28:29], v[12:13]
	s_nop 0
	v_pk_mul_f32 v[10:11], v[4:5], v[46:47]
	s_nop 0
	v_sub_f32_e32 v6, v10, v11
	v_pk_mul_f32 v[10:11], v[4:5], v[46:47] op_sel:[0,1] op_sel_hi:[1,0]
	s_waitcnt lgkmcnt(13)
	v_add_f32_e32 v44, v6, v14
	v_add_f32_e32 v6, v10, v11
	v_add_f32_e32 v42, v6, v15
	v_pk_mul_f32 v[10:11], v[4:5], v[42:43] op_sel:[1,0] op_sel_hi:[0,0]
	v_pk_fma_f32 v[12:13], v[4:5], v[44:45], v[10:11] neg_lo:[0,0,1] neg_hi:[0,0,1]
	v_pk_fma_f32 v[10:11], v[4:5], v[44:45], v[10:11] op_sel_hi:[1,0,1]
	s_nop 0
	v_mov_b32_e32 v13, v11
	s_waitcnt lgkmcnt(12)
	v_pk_add_f32 v[40:41], v[12:13], v[16:17]
	s_nop 0
	v_pk_mul_f32 v[10:11], v[4:5], v[40:41]
	s_nop 0
	v_sub_f32_e32 v6, v10, v11
	v_pk_mul_f32 v[10:11], v[4:5], v[40:41] op_sel:[0,1] op_sel_hi:[1,0]
	s_waitcnt lgkmcnt(11)
	v_add_f32_e32 v38, v6, v18
	v_add_f32_e32 v6, v10, v11
	v_add_f32_e32 v36, v6, v19
	v_pk_mul_f32 v[10:11], v[4:5], v[36:37] op_sel:[1,0] op_sel_hi:[0,0]
	v_pk_fma_f32 v[12:13], v[4:5], v[38:39], v[10:11] neg_lo:[0,0,1] neg_hi:[0,0,1]
	v_pk_fma_f32 v[10:11], v[4:5], v[38:39], v[10:11] op_sel_hi:[1,0,1]
	s_nop 0
	v_mov_b32_e32 v13, v11
	s_waitcnt lgkmcnt(10)
	v_pk_add_f32 v[34:35], v[12:13], v[20:21]
	s_nop 0
	v_pk_mul_f32 v[10:11], v[4:5], v[34:35]
	s_nop 0
	v_sub_f32_e32 v6, v10, v11
	v_pk_mul_f32 v[10:11], v[4:5], v[34:35] op_sel:[0,1] op_sel_hi:[1,0]
	s_waitcnt lgkmcnt(9)
	v_add_f32_e32 v32, v6, v22
	v_add_f32_e32 v6, v10, v11
	v_add_f32_e32 v30, v6, v23
	v_pk_mul_f32 v[10:11], v[4:5], v[30:31] op_sel:[1,0] op_sel_hi:[0,0]
	v_pk_fma_f32 v[12:13], v[4:5], v[32:33], v[10:11] neg_lo:[0,0,1] neg_hi:[0,0,1]
	v_pk_fma_f32 v[10:11], v[4:5], v[32:33], v[10:11] op_sel_hi:[1,0,1]
	s_nop 0
	v_mov_b32_e32 v13, v11
	s_waitcnt lgkmcnt(8)
	v_pk_add_f32 v[28:29], v[12:13], v[24:25]
	s_nop 0
	v_pk_mul_f32 v[10:11], v[4:5], v[28:29]
	s_nop 0
	v_sub_f32_e32 v6, v10, v11
	v_pk_mul_f32 v[10:11], v[4:5], v[28:29] op_sel:[0,1] op_sel_hi:[1,0]
	s_waitcnt lgkmcnt(7)
	v_add_f32_e32 v26, v6, v26
	v_add_f32_e32 v6, v10, v11
	v_add_f32_e32 v24, v6, v27
	v_pk_mul_f32 v[10:11], v[4:5], v[24:25] op_sel:[1,0] op_sel_hi:[0,0]
	v_pk_fma_f32 v[12:13], v[4:5], v[26:27], v[10:11] neg_lo:[0,0,1] neg_hi:[0,0,1]
	v_pk_fma_f32 v[10:11], v[4:5], v[26:27], v[10:11] op_sel_hi:[1,0,1]
	s_nop 0
	v_mov_b32_e32 v13, v11
	s_waitcnt lgkmcnt(6)
	v_pk_add_f32 v[22:23], v[12:13], v[54:55]
	s_nop 0
	v_pk_mul_f32 v[10:11], v[4:5], v[22:23]
	s_nop 0
	v_sub_f32_e32 v6, v10, v11
	v_pk_mul_f32 v[10:11], v[4:5], v[22:23] op_sel:[0,1] op_sel_hi:[1,0]
	s_waitcnt lgkmcnt(5)
	v_add_f32_e32 v20, v6, v56
	v_add_f32_e32 v6, v10, v11
	v_add_f32_e32 v18, v6, v57
	v_pk_mul_f32 v[10:11], v[4:5], v[18:19] op_sel:[1,0] op_sel_hi:[0,0]
	v_pk_fma_f32 v[12:13], v[4:5], v[20:21], v[10:11] neg_lo:[0,0,1] neg_hi:[0,0,1]
	v_pk_fma_f32 v[10:11], v[4:5], v[20:21], v[10:11] op_sel_hi:[1,0,1]
	s_nop 0
	v_mov_b32_e32 v13, v11
	s_waitcnt lgkmcnt(4)
	v_pk_add_f32 v[16:17], v[12:13], v[58:59]
	s_nop 0
	v_pk_mul_f32 v[10:11], v[4:5], v[16:17]
	s_nop 0
	v_sub_f32_e32 v6, v10, v11
	v_pk_mul_f32 v[10:11], v[4:5], v[16:17] op_sel:[0,1] op_sel_hi:[1,0]
	s_waitcnt lgkmcnt(3)
	v_add_f32_e32 v14, v6, v60
	v_add_f32_e32 v6, v10, v11
	v_add_f32_e32 v12, v6, v61
	v_pk_mul_f32 v[10:11], v[4:5], v[12:13] op_sel:[1,0] op_sel_hi:[0,0]
	v_pk_fma_f32 v[54:55], v[4:5], v[14:15], v[10:11] neg_lo:[0,0,1] neg_hi:[0,0,1]
	v_pk_fma_f32 v[10:11], v[4:5], v[14:15], v[10:11] op_sel_hi:[1,0,1]
	v_mov_b32_e32 v13, 0
	v_mov_b32_e32 v55, v11
	s_waitcnt lgkmcnt(2)
	v_pk_add_f32 v[10:11], v[54:55], v[62:63]
	s_nop 0
	v_pk_mul_f32 v[54:55], v[4:5], v[10:11]
	s_nop 0
	v_sub_f32_e32 v6, v54, v55
	v_pk_mul_f32 v[54:55], v[4:5], v[10:11] op_sel:[0,1] op_sel_hi:[1,0]
	s_waitcnt lgkmcnt(1)
	v_add_f32_e32 v8, v6, v64
	v_add_f32_e32 v6, v54, v55
	v_add_f32_e32 v6, v6, v65
	v_pk_mul_f32 v[54:55], v[4:5], v[6:7] op_sel:[1,0] op_sel_hi:[0,0]
	v_pk_fma_f32 v[56:57], v[4:5], v[8:9], v[54:55] neg_lo:[0,0,1] neg_hi:[0,0,1]
	v_pk_fma_f32 v[54:55], v[4:5], v[8:9], v[54:55] op_sel_hi:[1,0,1]
	s_nop 0
	v_mov_b32_e32 v57, v55
	s_waitcnt lgkmcnt(0)
	v_pk_add_f32 v[54:55], v[56:57], v[66:67]
	ds_write_b64 v31, v[54:55]
	s_waitcnt lgkmcnt(0)
	s_barrier
	s_and_saveexec_b64 s[38:39], vcc
	s_cbranch_execz .LBB0_787
	v_pk_mul_f32 v[52:53], v[4:5], v[4:5]
	v_add_f32_e32 v15, v4, v4
	v_sub_f32_e32 v13, v52, v53
	v_mul_f32_e32 v15, v5, v15
	v_mul_f32_e32 v19, v13, v13
	v_add_f32_e32 v13, v13, v13
	v_mul_f32_e32 v13, v15, v13
	v_fma_f32 v19, -v15, v15, v19
	v_mul_f32_e32 v15, v13, v13
	v_fma_f32 v15, v19, v19, -v15
	v_add_f32_e32 v19, v19, v19
	v_mul_f32_e32 v13, v13, v19
	v_mul_f32_e32 v19, v13, v13
	v_fma_f32 v52, v15, v15, -v19
	v_add_f32_e32 v15, v15, v15
	v_mul_f32_e32 v54, v13, v15
	v_mov_b32_e32 v56, 0
	v_lshl_add_u32 v9, v9, 2, 0
	v_mov_b32_e32 v53, v52
	v_mov_b32_e32 v55, v54
	s_mov_b64 s[42:43], 0
	v_mov_b32_e32 v13, v3
	v_mov_b32_e32 v57, v56

.LBB0_787:
	s_or_b64 exec, exec, s[38:39]
	v_lshl_or_b32 v54, v3, 11, v7
	v_readlane_b32 s18, v251, 59
	v_ashrrev_i32_e32 v55, 31, v54
	v_readlane_b32 s19, v251, 60
	v_add_f32_e32 v3, v53, v50
	v_cvt_pk_bf16_f32 v3, v3, s0
	v_lshl_add_u64 v[54:55], v[54:55], 1, s[18:19]
	global_store_short v[54:55], v13, off
	global_store_short_d16_hi v[54:55], v13, off offset:128
	global_store_short v[54:55], v3, off offset:256
	v_add_f32_e32 v3, v52, v48
	v_cvt_pk_bf16_f32 v3, v3, s0
	global_store_short v[54:55], v3, off offset:384
	v_mul_f32_e32 v3, v4, v53
	v_fma_f32 v3, -v5, v52, v3
	v_add_f32_e32 v7, v3, v46
	v_pk_mul_f32 v[48:49], v[4:5], v[52:53]
	v_cvt_pk_bf16_f32 v7, v7, s0
	global_store_short v[54:55], v7, off offset:512
	v_add_f32_e32 v7, v48, v49
	v_add_f32_e32 v9, v7, v47
	v_cvt_pk_bf16_f32 v9, v9, s0
	global_store_short v[54:55], v9, off offset:640
	v_mul_f32_e32 v9, v4, v3
	v_fma_f32 v9, -v5, v7, v9
	v_mul_f32_e32 v7, v4, v7
	v_fmac_f32_e32 v7, v5, v3
	v_add_f32_e32 v3, v9, v44
	v_cvt_pk_bf16_f32 v3, v3, s0
	global_store_short v[54:55], v3, off offset:768
	v_add_f32_e32 v3, v7, v42
	v_cvt_pk_bf16_f32 v3, v3, s0
	global_store_short v[54:55], v3, off offset:896
	v_mul_f32_e32 v3, v4, v9
	v_fma_f32 v3, -v5, v7, v3
	v_mul_f32_e32 v7, v4, v7
	v_fmac_f32_e32 v7, v5, v9
	v_add_f32_e32 v9, v7, v41
	v_cvt_pk_bf16_f32 v9, v9, s0
	global_store_short v[54:55], v9, off offset:1152
	v_mul_f32_e32 v9, v4, v3
	v_fma_f32 v9, -v5, v7, v9
	v_mul_f32_e32 v7, v4, v7
	v_add_f32_e32 v13, v3, v40
	v_fmac_f32_e32 v7, v5, v3
	v_add_f32_e32 v3, v9, v38
	v_cvt_pk_bf16_f32 v3, v3, s0
	global_store_short v[54:55], v3, off offset:1280
	v_add_f32_e32 v3, v7, v36
	v_cvt_pk_bf16_f32 v3, v3, s0
	global_store_short v[54:55], v3, off offset:1408
	v_mul_f32_e32 v3, v4, v9
	v_fma_f32 v3, -v5, v7, v3
	v_mul_f32_e32 v7, v4, v7
	v_fmac_f32_e32 v7, v5, v9
	v_add_f32_e32 v9, v7, v35
	v_cvt_pk_bf16_f32 v9, v9, s0
	global_store_short v[54:55], v9, off offset:1664
	v_mul_f32_e32 v9, v4, v3
	v_cvt_pk_bf16_f32 v13, v13, s0
	v_fma_f32 v9, -v5, v7, v9
	v_mul_f32_e32 v7, v4, v7
	global_store_short v[54:55], v13, off offset:1024
	v_add_f32_e32 v13, v3, v34
	v_fmac_f32_e32 v7, v5, v3
	v_add_f32_e32 v3, v9, v32
	v_cvt_pk_bf16_f32 v3, v3, s0
	global_store_short v[54:55], v3, off offset:1792
	v_add_f32_e32 v3, v7, v30
	v_cvt_pk_bf16_f32 v3, v3, s0
	global_store_short v[54:55], v3, off offset:1920
	v_mul_f32_e32 v3, v4, v9
	v_fma_f32 v3, -v5, v7, v3
	v_mul_f32_e32 v7, v4, v7
	v_fmac_f32_e32 v7, v5, v9
	v_add_f32_e32 v9, v7, v29
	v_cvt_pk_bf16_f32 v9, v9, s0
	global_store_short v[54:55], v9, off offset:2176
	v_mul_f32_e32 v9, v4, v3
	v_cvt_pk_bf16_f32 v13, v13, s0
	v_fma_f32 v9, -v5, v7, v9
	v_mul_f32_e32 v7, v4, v7
	global_store_short v[54:55], v13, off offset:1536
	v_add_f32_e32 v13, v3, v28
	v_fmac_f32_e32 v7, v5, v3
	v_add_f32_e32 v3, v9, v26
	v_cvt_pk_bf16_f32 v3, v3, s0
	global_store_short v[54:55], v3, off offset:2304
	v_add_f32_e32 v3, v7, v24
	v_cvt_pk_bf16_f32 v3, v3, s0
	global_store_short v[54:55], v3, off offset:2432
	v_mul_f32_e32 v3, v4, v9
	v_fma_f32 v3, -v5, v7, v3
	v_mul_f32_e32 v7, v4, v7
	v_fmac_f32_e32 v7, v5, v9
	v_add_f32_e32 v9, v7, v23
	v_cvt_pk_bf16_f32 v9, v9, s0
	global_store_short v[54:55], v9, off offset:2688
	v_mul_f32_e32 v9, v4, v3
	v_cvt_pk_bf16_f32 v13, v13, s0
	v_fma_f32 v9, -v5, v7, v9
	v_mul_f32_e32 v7, v4, v7
	global_store_short v[54:55], v13, off offset:2048
	v_add_f32_e32 v13, v3, v22
	v_fmac_f32_e32 v7, v5, v3
	v_add_f32_e32 v3, v9, v20
	v_cvt_pk_bf16_f32 v3, v3, s0
	global_store_short v[54:55], v3, off offset:2816
	v_add_f32_e32 v3, v7, v18
	v_cvt_pk_bf16_f32 v3, v3, s0
	global_store_short v[54:55], v3, off offset:2944
	v_mul_f32_e32 v3, v4, v9
	v_fma_f32 v3, -v5, v7, v3
	v_mul_f32_e32 v7, v4, v7
	v_fmac_f32_e32 v7, v5, v9
	v_add_f32_e32 v9, v7, v17
	v_cvt_pk_bf16_f32 v9, v9, s0
	global_store_short v[54:55], v9, off offset:3200
	v_mul_f32_e32 v9, v4, v3
	v_cvt_pk_bf16_f32 v13, v13, s0
	v_fma_f32 v9, -v5, v7, v9
	v_mul_f32_e32 v7, v4, v7
	global_store_short v[54:55], v13, off offset:2560
	v_add_f32_e32 v13, v3, v16
	v_fmac_f32_e32 v7, v5, v3
	v_add_f32_e32 v3, v9, v14
	v_cvt_pk_bf16_f32 v3, v3, s0
	global_store_short v[54:55], v3, off offset:3328
	v_add_f32_e32 v3, v7, v12
	v_cvt_pk_bf16_f32 v3, v3, s0
	global_store_short v[54:55], v3, off offset:3456
	v_mul_f32_e32 v3, v4, v9
	v_fma_f32 v3, -v5, v7, v3
	v_mul_f32_e32 v7, v4, v7
	v_fmac_f32_e32 v7, v5, v9
	v_add_f32_e32 v9, v7, v11
	v_cvt_pk_bf16_f32 v9, v9, s0
	global_store_short v[54:55], v9, off offset:3712
	v_mul_f32_e32 v9, v4, v3
	v_fma_f32 v9, -v5, v7, v9
	v_mul_f32_e32 v4, v4, v7
	v_add_f32_e32 v10, v3, v10
	v_fmac_f32_e32 v4, v5, v3
	v_add_f32_e32 v3, v9, v8
	v_cvt_pk_bf16_f32 v3, v3, s0
	global_store_short v[54:55], v3, off offset:3840
	v_add_f32_e32 v3, v4, v6
	v_cvt_pk_bf16_f32 v13, v13, s0
	v_cvt_pk_bf16_f32 v10, v10, s0
	v_cvt_pk_bf16_f32 v3, v3, s0
	global_store_short v[54:55], v13, off offset:3072
	global_store_short v[54:55], v10, off offset:3584
	global_store_short v[54:55], v3, off offset:3968
	v_mov_b32_e32 v58, v0
	s_barrier
	v_readlane_b32 s26, v249, 45
	v_lshlrev_b32_e32 v3, 3, v58
	v_ashrrev_i32_e32 v56, 4, v58
	v_and_b32_e32 v84, 0x78, v3
	v_or_b32_e32 v178, s26, v84
	v_ashrrev_i32_e32 v57, 31, v56
	v_readlane_b32 s26, v249, 40
	v_readlane_b32 s27, v249, 41
	v_lshlrev_b64 v[8:9], 8, v[56:57]
	v_readfirstlane_b32 s12, v58
	s_mov_b64 s[38:39], -1
	s_and_b64 vcc, s[26:27], exec
	v_lshl_add_u64 v[160:161], s[18:19], 0, v[8:9]
	v_add_u32_e32 v16, 0xffffff00, v178
	s_cbranch_vccz .LBB0_789
	v_readlane_b32 s18, v251, 59
	v_readlane_b32 s19, v251, 60
	v_add_u32_e32 v6, 0xffffff00, v178
	s_mov_b64 s[38:39], 0
	v_lshl_add_u64 v[4:5], s[18:19], 0, v[8:9]
